# best + nt on P3/P4 attention q/k/v loads (K/V tile DMA + q fragments)
# speedup vs baseline: 1.0195x; 1.0195x over previous
; DI int tr_base(int rlane, int cch, int q, int p) { return img_off(rlane + q, cch + (p >> 1)) + 8 * (p & 1); }
; #define ATT_DECODE(k_, b_, hd_, res_, ib_) do { const int u_ = F.vcu + (k_) * F.G; const int bh_ = u_ >> 4, uu_ = u_ & 15; b_ = bh_ >> 3; hd_ = bh_ & 7; res_ = uu_ / BPR; ib_ = (uu_ % BPR) * 1024; } while (0)
; template <int DIL, bool FIRST, bool LAST>
; DI void attn_phase(Frame& F) {
;     ...
;     const int lane = F.lane, r = lane & 31, h = lane >> 5, g = lane >> 4, i16 = lane & 15, q4 = i16 >> 2, p4 = i16 & 3;
;     const int prow = 4 * F.wave + g, pch = i16 ^ ((g << 2) | (F.wave & 3));
;     const unsigned pdst = (unsigned)F.wave * 1024u;
;     int vB0[4], vB1[4];
; #pragma unroll
;     for (int db = 0; db < 4; ++db) { vB0[db] = tr_base(4 * h, 4 * db + 2 * (g & 1), q4, p4); vB1[db] = tr_base(8 + 4 * h, 4 * db + 2 * (g & 1), q4, p4); }
;     const int kmask = ((r & 3) << 2) | ((r >> 2) & 3);
;     __syncthreads();
;     const int nun = (F.vcu < 256) ? (255 - F.vcu) / F.G + 1 : 0;
;     if (nun > 0) {
;     ...
;         int iu = 0, ij = 0, is = 0, ib_i; const bf16* kv_i;
;         { int b_, hd_, res_; ATT_DECODE(0, b_, hd_, res_, ib_i); kv_i = HMq + HM_PLANE + ((size_t)(b_ * 8 + hd_) * SEQ + res_) * 128; }
;     ...
;         u32x4 qfr[8], on[8]; u32x2 mlx; mlx.x = 0u; mlx.y = 0u;
;     ...
;         ATT_PREFETCH(0, F.wave);
; #pragma unroll
;         for (int jt = 0; jt < PRE; ++jt) ATT_ISSUE1();
.LBB0_362:
	s_cmp_lt_i32 s33, 1
	s_cbranch_scc1 .LBB0_394
	v_writelane_b32 v254, s76, 47
	s_add_u32 s0, s94, 0x6c000000
	s_addc_u32 s1, s95, 0
	v_writelane_b32 v254, s77, 48
	v_lshrrev_b32_e32 v2, 2, v105
	v_lshlrev_b32_e32 v12, 2, v130
	v_lshlrev_b32_e32 v3, 1, v104
	v_writelane_b32 v254, s0, 49
	v_and_b32_e32 v3, 2, v3
	v_or_b32_e32 v4, v12, v2
	v_or_b32_e32 v6, v130, v108
	v_or_b32_e32 v13, 8, v12
	v_writelane_b32 v254, s1, 50
	s_bfe_u32 s0, s78, 0x20006
	v_or_b32_e32 v5, v3, v107
	v_lshl_or_b32 v4, v4, 8, v109
	v_or_b32_e32 v2, v13, v2
	v_lshrrev_b32_e32 v8, 2, v13
	v_bitop3_b32 v3, v3, v6, v107 bitop3:0x36
	v_lshl_or_b32 v2, v2, 8, v109
	v_lshl_or_b32 v164, v3, 4, v4
	v_bitop3_b32 v3, v8, v5, v108 bitop3:0x36
	s_add_u32 s76, s94, 0xa7400000
	v_or_b32_e32 v9, v8, v108
	v_lshl_add_u32 v165, v3, 4, v2
	v_bitop3_b32 v3, v5, v6, 4 bitop3:0x36
	s_addc_u32 s77, s95, 0
	s_lshl_b32 s1, s85, 10
	v_lshl_or_b32 v166, v3, 4, v4
	v_bitop3_b32 v3, v5, v9, 4 bitop3:0x36
	s_and_b32 s72, s1, 0x3c00
	s_ashr_i32 s1, s85, 4
	v_bitop3_b32 v7, s0, v105, v106 bitop3:0x36
	v_lshl_add_u32 v167, v3, 4, v2
	v_bitop3_b32 v3, v5, v6, 8 bitop3:0x36
	s_bfe_u32 s0, s85, 0x30004
	s_and_b32 s1, s1, -8
	v_lshl_or_b32 v168, v3, 4, v4
	v_bitop3_b32 v3, v5, v9, 8 bitop3:0x36
	s_or_b32 s0, s1, s0
	v_lshl_add_u32 v169, v3, 4, v2
	v_bitop3_b32 v3, v5, v6, 12 bitop3:0x36
	v_readlane_b32 s70, v254, 23
	s_ashr_i32 s1, s0, 31
	v_lshl_or_b32 v170, v3, 4, v4
	v_bitop3_b32 v3, v5, v9, 12 bitop3:0x36
	s_lshl_b64 s[2:3], s[0:1], 22
	s_lshl_b32 s0, s70, 5
	v_lshl_add_u32 v171, v3, 4, v2
	s_lshl_b32 s6, s70, 10
	v_lshlrev_b32_e32 v2, 2, v0
	s_add_i32 s1, s72, s0
	v_and_b32_e32 v15, 12, v2
	v_or_b32_e32 v2, s1, v1
	v_mov_b32_e32 v3, 0
	s_add_u32 s4, s76, s2
	s_addc_u32 s5, s77, s3
	v_lshlrev_b64 v[4:5], 8, v[2:3]
	v_lshl_add_u64 v[4:5], s[4:5], 0, v[4:5]
	v_lshlrev_b32_e32 v2, 4, v130
	v_lshl_add_u64 v[4:5], v[4:5], 0, v[2:3]
	global_load_dwordx4 v[98:101], v[4:5], off offset:0 nt
	v_or_b32_e32 v14, s26, v104
	global_load_dwordx4 v[102:105], v[4:5], off offset:32 nt
	global_load_dwordx4 v[106:109], v[4:5], off offset:64 nt
	global_load_dwordx4 v[110:113], v[4:5], off offset:0x60 nt
	global_load_dwordx4 v[114:117], v[4:5], off offset:0x80
	global_load_dwordx4 v[118:121], v[4:5], off offset:0xa0
	global_load_dwordx4 v[122:125], v[4:5], off offset:0xc0
	s_add_u32 s1, s94, 0xab400000
	v_add_u32_e32 v172, 0xffffff80, v14
	global_load_dwordx4 v[126:129], v[4:5], off offset:0xe0
	s_addc_u32 s4, s95, 0
	v_add_u32_e32 v5, s72, v172
	s_add_u32 s80, s1, s2
	v_max_i32_e32 v8, 0, v5
	v_mov_b32_e32 v9, v3
	s_addc_u32 s81, s4, s3
	v_lshlrev_b64 v[8:9], 8, v[8:9]
	v_lshl_add_u64 v[8:9], s[80:81], 0, v[8:9]
	v_lshlrev_b32_e32 v10, 4, v7
	v_mov_b32_e32 v11, v3
	v_lshl_add_u64 v[8:9], v[8:9], 0, v[10:11]
	s_mov_b64 s[82:83], 0x4000000
	v_lshlrev_b32_e32 v4, 3, v7
	s_add_i32 s97, s6, 0
	s_mov_b32 m0, s97
	global_load_lds_dwordx4 v[8:9], off nt
	v_lshl_add_u64 v[8:9], v[8:9], 0, s[82:83]
	v_max_i32_e32 v7, 0xffffffe0, v5
	v_writelane_b32 v254, s1, 51
	s_add_i32 s1, s97, 0x2000
	s_mov_b32 m0, s1
	global_load_lds_dwordx4 v[8:9], off nt
	v_add_u32_e32 v8, 32, v7
	v_mov_b32_e32 v9, v3
	v_lshlrev_b64 v[8:9], 8, v[8:9]
	v_lshl_add_u64 v[8:9], s[80:81], 0, v[8:9]
	v_lshl_add_u64 v[8:9], v[8:9], 0, v[10:11]
	s_add_i32 s1, s97, 0x4000
	s_mov_b32 m0, s1
	global_load_lds_dwordx4 v[8:9], off nt
	v_lshl_add_u64 v[8:9], v[8:9], 0, s[82:83]
	v_max_i32_e32 v7, 0xffffffc0, v5
	s_addk_i32 s1, 0x2000
	s_mov_b32 m0, s1
	global_load_lds_dwordx4 v[8:9], off nt
	v_add_u32_e32 v8, 64, v7
	v_mov_b32_e32 v9, v3
	v_lshlrev_b64 v[8:9], 8, v[8:9]
	v_lshl_add_u64 v[8:9], s[80:81], 0, v[8:9]
	v_lshl_add_u64 v[8:9], v[8:9], 0, v[10:11]
	s_add_i32 s1, s97, 0x8000
	s_mov_b32 m0, s1
	global_load_lds_dwordx4 v[8:9], off nt
	v_lshl_add_u64 v[8:9], v[8:9], 0, s[82:83]
	v_max_i32_e32 v7, 0xffffffa0, v5
	s_addk_i32 s1, 0x2000
	s_mov_b32 m0, s1
	global_load_lds_dwordx4 v[8:9], off nt
	v_add_u32_e32 v8, 0x60, v7
	v_mov_b32_e32 v9, v3
	v_lshlrev_b64 v[8:9], 8, v[8:9]
	v_lshl_add_u64 v[8:9], s[80:81], 0, v[8:9]
	v_lshl_add_u64 v[8:9], v[8:9], 0, v[10:11]
	s_add_i32 s1, s97, 0xc000
	s_mov_b32 m0, s1
	global_load_lds_dwordx4 v[8:9], off nt
	v_lshl_add_u64 v[8:9], v[8:9], 0, s[82:83]
	s_addk_i32 s1, 0x2000
	s_mov_b32 m0, s1
; DI int crow(int reg, int h) { return (reg & 3) + 8 * (reg >> 2) + 4 * h; }
; template <int DIL, bool FIRST, bool LAST>
; DI void attn_phase(Frame& F) {
;     ...
;                     { const int kb = i0 - 128 + 32 * kt;
;                       if (kt == 0 || kt == 4 || kb < 0) {
; #pragma unroll
;                         for (int e = 0; e < 16; ++e) { const int ce = crow(e, h); const bool bad = ((kb + ce) < 0) || (kt == 0 && ce < r) || (kt == 4 && ce > r); if (bad) s[e] = -1e30f; } } }
	global_load_lds_dwordx4 v[8:9], off nt
	v_add_u32_e32 v8, s72, v14
	v_mov_b32_e32 v9, v3
	v_lshlrev_b64 v[8:9], 8, v[8:9]
	v_lshl_add_u64 v[8:9], s[80:81], 0, v[8:9]
	v_lshl_add_u64 v[8:9], v[8:9], 0, v[10:11]
	s_add_i32 s1, s97, 0x10000
	s_mov_b32 m0, s1
	global_load_lds_dwordx4 v[8:9], off nt
	v_lshl_add_u64 v[8:9], v[8:9], 0, s[82:83]
	v_max_i32_e32 v5, 0xffffff60, v5
	v_or_b32_e32 v16, v15, v131
	s_addk_i32 s1, 0x2000
	s_mov_b32 m0, s1
	global_load_lds_dwordx4 v[8:9], off nt
	v_add_u32_e32 v8, 0xa0, v5
	v_bitop3_b32 v5, v15, v130, v131 bitop3:0x36
	v_lshlrev_b32_e32 v174, 4, v5
	v_bitop3_b32 v5, v130, v16, 2 bitop3:0x36
	v_lshlrev_b32_e32 v175, 4, v5
	v_bitop3_b32 v5, v130, v16, 4 bitop3:0x36
	v_lshlrev_b32_e32 v176, 4, v5
	v_bitop3_b32 v5, v130, v16, 6 bitop3:0x36
	v_lshlrev_b32_e32 v177, 4, v5
	v_bitop3_b32 v5, v130, v16, 8 bitop3:0x36
	v_lshlrev_b32_e32 v178, 4, v5
	v_bitop3_b32 v5, v130, v16, 10 bitop3:0x36
	v_lshlrev_b32_e32 v179, 4, v5
	v_bitop3_b32 v5, v130, v16, 12 bitop3:0x36
	v_lshlrev_b32_e32 v180, 4, v5
	v_bitop3_b32 v5, v130, v16, 14 bitop3:0x36
	v_lshlrev_b32_e32 v181, 4, v5
	v_or_b32_e32 v5, 1, v12
	v_cmp_lt_u32_e64 s[8:9], v5, v1
	v_or_b32_e32 v5, 2, v12
	v_mov_b32_e32 v9, v3
	v_cmp_lt_u32_e64 s[12:13], v5, v1
	v_cmp_gt_u32_e64 s[14:15], v5, v1
	v_or_b32_e32 v5, 3, v12
	v_lshlrev_b64 v[8:9], 8, v[8:9]
	v_cmp_lt_u32_e64 s[16:17], v5, v1
	v_cmp_gt_u32_e64 s[18:19], v5, v1
	v_or_b32_e32 v5, 9, v12
	v_lshl_add_u64 v[8:9], s[80:81], 0, v[8:9]
	v_cmp_lt_u32_e64 s[24:25], v5, v1
	v_cmp_gt_u32_e64 s[26:27], v5, v1
	v_or_b32_e32 v5, 10, v12
	v_lshl_add_u64 v[8:9], v[8:9], 0, v[10:11]
	v_cmp_lt_u32_e64 s[28:29], v5, v1
	v_cmp_gt_u32_e64 s[30:31], v5, v1
	v_or_b32_e32 v5, 11, v12
	s_add_i32 s1, s97, 0x14000
	s_mov_b32 m0, s1
	global_load_lds_dwordx4 v[8:9], off nt
	v_lshl_add_u64 v[8:9], v[8:9], 0, s[82:83]
	v_cmp_lt_u32_e64 s[34:35], v5, v1
	v_cmp_gt_u32_e64 s[36:37], v5, v1
	v_or_b32_e32 v5, 16, v12
	s_addk_i32 s1, 0x2000
	s_mov_b32 m0, s1
	global_load_lds_dwordx4 v[8:9], off nt
	v_lshl_add_u64 v[8:9], s[94:95], 0, v[2:3]
	s_mov_b64 s[2:3], 0x64000000
	v_cmp_lt_u32_e64 s[38:39], v5, v1
	v_cmp_gt_u32_e64 s[40:41], v5, v1
	v_or_b32_e32 v5, 17, v12
	v_writelane_b32 v254, s4, 52
	v_lshl_add_u64 v[150:151], v[8:9], 0, s[2:3]
	v_cmp_gt_u32_e64 s[2:3], 32, v224
	v_cmp_lt_u32_e64 s[42:43], v5, v1
	v_cmp_gt_u32_e64 s[44:45], v5, v1
	v_or_b32_e32 v5, 18, v12
	v_writelane_b32 v254, s2, 54
	v_cmp_lt_u32_e64 s[46:47], v5, v1
	v_cmp_gt_u32_e64 s[48:49], v5, v1
	v_or_b32_e32 v5, 19, v12
	v_writelane_b32 v254, s3, 55
	v_cmp_lt_u32_e64 s[2:3], v12, v1
	v_cmp_lt_u32_e64 s[50:51], v5, v1
	v_cmp_gt_u32_e64 s[52:53], v5, v1
	v_or_b32_e32 v5, 24, v12
	v_writelane_b32 v254, s2, 56
	v_cmp_lt_u32_e64 s[54:55], v5, v1
	v_cmp_gt_u32_e64 s[56:57], v5, v1
	v_or_b32_e32 v5, 25, v12
	v_writelane_b32 v254, s3, 57
	v_cmp_lt_u32_e64 s[58:59], v5, v1
	v_cmp_gt_u32_e64 s[60:61], v5, v1
	v_or_b32_e32 v5, 26, v12
	v_lshlrev_b32_e32 v6, 3, v130
	v_cmp_lt_u32_e64 s[62:63], v5, v1
	v_cmp_gt_u32_e64 s[64:65], v5, v1
	v_or_b32_e32 v5, 27, v12
	v_writelane_b32 v254, s76, 58
	s_mov_b32 s74, 0
	v_lshlrev_b32_e32 v173, 8, v1
	v_lshl_add_u64 v[152:153], s[76:77], 0, v[2:3]
	v_mbcnt_lo_u32_b32 v2, -1, 0
	s_mov_b32 s75, 6
	v_sub_u32_e32 v182, 0, v12
	v_cmp_gt_u32_e64 s[6:7], v12, v1
	v_cmp_ge_u32_e64 s[10:11], v12, v1
	v_sub_u32_e32 v183, -8, v12
	v_cmp_lt_u32_e64 s[20:21], v13, v1
	v_cmp_gt_u32_e64 s[22:23], v13, v1
	v_sub_u32_e32 v184, -9, v12
	v_sub_u32_e32 v185, -10, v12
	v_sub_u32_e32 v186, -11, v12
	v_sub_u32_e32 v187, -16, v12
	v_sub_u32_e32 v188, 0xffffffef, v12
	v_sub_u32_e32 v189, 0xffffffee, v12
	v_sub_u32_e32 v190, 0xffffffed, v12
	v_sub_u32_e32 v191, 0xffffffe8, v12
	v_sub_u32_e32 v192, 0xffffffe7, v12
	v_sub_u32_e32 v193, 0xffffffe6, v12
	v_sub_u32_e32 v194, 0xffffffe5, v12
	v_cmp_lt_u32_e64 s[66:67], v5, v1
	v_cmp_gt_u32_e64 s[68:69], v5, v1
	v_or_b32_e32 v195, s0, v1
	v_writelane_b32 v254, s77, 59
	v_or_b32_e32 v196, 0x100, v1
	s_sub_i32 s78, 0, s70
	v_mov_b32_e32 v197, 0xf149f2ca
	v_lshlrev_b32_e32 v154, 1, v6
	v_lshlrev_b32_e32 v156, 1, v4
	v_mbcnt_hi_u32_b32 v198, -1, v2
	s_mov_b32 s70, 6
	s_mov_b32 s71, 0
	v_mov_b32_e32 v158, 0xf149f2ca
	v_mov_b32_e32 v159, v3
	s_mov_b32 s4, 0
	s_waitcnt vmcnt(0)
	s_branch .LBB0_365

.LBB0_367:
	s_lshl_b32 s0, s75, 5
	s_add_i32 s0, s72, s0
	v_add_u32_e32 v2, s0, v172
	v_max_i32_e32 v2, 0, v2
	v_lshlrev_b64 v[4:5], 8, v[2:3]
	v_lshl_add_u64 v[4:5], s[80:81], 0, v[4:5]
	v_mov_b32_e32 v157, v3
	s_and_b32 s0, s86, 0x1c000
	v_lshl_add_u64 v[4:5], v[4:5], 0, v[156:157]
	s_add_i32 s0, s97, s0
	s_mov_b32 m0, s0
	global_load_lds_dwordx4 v[4:5], off nt
	v_lshl_add_u64 v[4:5], v[4:5], 0, s[82:83]
	s_addk_i32 s0, 0x2000
	s_mov_b32 m0, s0
	global_load_lds_dwordx4 v[4:5], off nt
	s_add_i32 s75, s75, 1
	s_cmp_lg_u32 s75, 36
	s_cbranch_scc1 .LBB0_370
	s_add_i32 s0, s74, 1
	s_cmp_ge_i32 s0, s33
	s_mov_b32 s75, 35
	s_cbranch_scc1 .LBB0_370
	v_readlane_b32 s1, v254, 2
	s_mul_i32 s1, s0, s1
	v_readlane_b32 s2, v254, 43
	s_add_i32 s1, s1, s2
	s_bfe_u32 s2, s1, 0x30004
	s_lshl_b32 s3, s1, 10
	s_ashr_i32 s1, s1, 4
	s_and_b32 s1, s1, -8
	s_or_b32 s2, s1, s2
	s_and_b32 s72, s3, 0x3c00
	s_ashr_i32 s3, s2, 31
	s_lshl_b64 s[2:3], s[2:3], 22
	v_readlane_b32 s1, v254, 51
	s_add_u32 s80, s1, s2
	v_readlane_b32 s1, v254, 52
	s_addc_u32 s81, s1, s3
	s_mov_b32 s75, 0
	s_mov_b32 s74, s0

; template <int DIL, bool FIRST, bool LAST>
; DI void attn_phase(Frame& F) {
;     ...
;                         if (mq < 3) ATT_PREFETCH(k, qt + 8); else if (k + 1 < nun) ATT_PREFETCH(k + 1, F.wave);
.LBB0_389:
	v_readlane_b32 s0, v254, 61
	v_readlane_b32 s1, v254, 62
	s_andn2_b64 vcc, exec, s[0:1]
	s_cbranch_vccnz .LBB0_391
	global_load_dwordx4 v[98:101], v[160:161], off offset:0 nt
	global_load_dwordx4 v[102:105], v[160:161], off offset:32 nt
	global_load_dwordx4 v[106:109], v[160:161], off offset:64 nt
	global_load_dwordx4 v[110:113], v[160:161], off offset:0x60 nt
	global_load_dwordx4 v[114:117], v[160:161], off offset:0x80
	global_load_dwordx4 v[118:121], v[160:161], off offset:0xa0
	global_load_dwordx4 v[122:125], v[160:161], off offset:0xc0
	global_load_dwordx4 v[126:129], v[160:161], off offset:0xe0

; template <int DIL, bool FIRST, bool LAST>
; DI void attn_phase(Frame& F) {
;     ...
;                         if (mq < 3) ATT_PREFETCH(k, qt + 8); else if (k + 1 < nun) ATT_PREFETCH(k + 1, F.wave);
.LBB0_392:
	v_add_u32_e32 v4, s96, v155
	v_ashrrev_i32_e32 v5, 31, v4
	v_lshlrev_b64 v[4:5], 8, v[4:5]
	v_lshl_add_u64 v[4:5], v[162:163], 0, v[4:5]
	global_load_dwordx4 v[98:101], v[4:5], off offset:0 nt
	global_load_dwordx4 v[102:105], v[4:5], off offset:32 nt
	global_load_dwordx4 v[106:109], v[4:5], off offset:64 nt
	global_load_dwordx4 v[110:113], v[4:5], off offset:0x60 nt
	global_load_dwordx4 v[114:117], v[4:5], off offset:0x80
	global_load_dwordx4 v[118:121], v[4:5], off offset:0xa0
	global_load_dwordx4 v[122:125], v[4:5], off offset:0xc0
	global_load_dwordx4 v[126:129], v[4:5], off offset:0xe0
	s_branch .LBB0_366

; DI int tr_base(int rlane, int cch, int q, int p) { return img_off(rlane + q, cch + (p >> 1)) + 8 * (p & 1); }
; #define ATT_DECODE(k_, b_, hd_, res_, ib_) do { const int u_ = F.vcu + (k_) * F.G; const int bh_ = u_ >> 4, uu_ = u_ & 15; b_ = bh_ >> 3; hd_ = bh_ & 7; res_ = uu_ / BPR; ib_ = (uu_ % BPR) * 1024; } while (0)
; template <int DIL, bool FIRST, bool LAST>
; DI void attn_phase(Frame& F) {
;     ...
;     const int lane = F.lane, r = lane & 31, h = lane >> 5, g = lane >> 4, i16 = lane & 15, q4 = i16 >> 2, p4 = i16 & 3;
;     const int prow = 4 * F.wave + g, pch = i16 ^ ((g << 2) | (F.wave & 3));
;     const unsigned pdst = (unsigned)F.wave * 1024u;
;     int vB0[4], vB1[4];
; #pragma unroll
;     for (int db = 0; db < 4; ++db) { vB0[db] = tr_base(4 * h, 4 * db + 2 * (g & 1), q4, p4); vB1[db] = tr_base(8 + 4 * h, 4 * db + 2 * (g & 1), q4, p4); }
;     const int kmask = ((r & 3) << 2) | ((r >> 2) & 3);
;     __syncthreads();
;     const int nun = (F.vcu < 256) ? (255 - F.vcu) / F.G + 1 : 0;
;     if (nun > 0) {
;     ...
;         int iu = 0, ij = 0, is = 0, ib_i; const bf16* kv_i;
;         { int b_, hd_, res_; ATT_DECODE(0, b_, hd_, res_, ib_i); kv_i = HMq + HM_PLANE + ((size_t)(b_ * 8 + hd_) * SEQ + res_) * 128; }
;     ...
;         u32x4 qfr[8], on[8]; u32x2 mlx; mlx.x = 0u; mlx.y = 0u;
;     ...
;         ATT_PREFETCH(0, F.wave);
.LBB0_585:
	s_cmp_lt_i32 s72, 1
	s_cbranch_scc1 .LBB0_617
	v_writelane_b32 v254, s76, 58
	v_lshrrev_b32_e32 v2, 4, v224
	v_and_b32_e32 v3, 15, v0
	v_writelane_b32 v254, s77, 59
	s_add_u32 s76, s94, 0x6c000000
	s_addc_u32 s77, s95, 0
	v_lshlrev_b32_e32 v4, 2, v2
	s_bfe_u32 s0, s78, 0x20006
	v_bitop3_b32 v9, s0, v3, v4 bitop3:0x36
	s_add_u32 s0, s94, 0x64000000
	s_addc_u32 s1, s95, 0
	s_add_u32 s2, s94, 0xa7400000
	s_addc_u32 s3, s95, 0
	v_readlane_b32 s70, v254, 23
	s_lshl_b32 s5, s85, 10
	s_lshl_b32 s8, s70, 10
	s_bfe_u32 s4, s85, 0x30004
	s_and_b32 s75, s5, 0xc00
	v_bfe_u32 v8, v0, 2, 2
	v_lshlrev_b32_e32 v10, 2, v222
	v_lshrrev_b32_e32 v3, 3, v224
	v_and_b32_e32 v7, 12, v0
	v_lshlrev_b32_e32 v12, 3, v0
	s_add_u32 s9, s94, 0xab400000
	v_and_b32_e32 v3, 2, v3
	v_or_b32_e32 v4, v10, v8
	v_bfe_u32 v5, v0, 1, 1
	v_or_b32_e32 v11, v222, v7
	v_and_b32_e32 v12, 8, v12
	v_or_b32_e32 v13, 8, v10
	s_addc_u32 s10, s95, 0
	s_ashr_i32 s5, s85, 4
	v_or_b32_e32 v6, v3, v5
	v_lshl_or_b32 v4, v4, 8, v12
	v_or_b32_e32 v14, v13, v8
	v_lshrrev_b32_e32 v15, 2, v13
	v_bitop3_b32 v3, v3, v11, v5 bitop3:0x36
	s_and_b32 s5, s5, -8
	v_lshl_or_b32 v12, v14, 8, v12
	v_lshl_or_b32 v196, v3, 4, v4
	v_bitop3_b32 v3, v15, v6, v7 bitop3:0x36
	s_or_b32 s4, s5, s4
	v_or_b32_e32 v16, v15, v7
	v_lshl_add_u32 v197, v3, 4, v12
	v_bitop3_b32 v3, v6, v11, 4 bitop3:0x36
	s_ashr_i32 s5, s4, 31
	v_lshl_or_b32 v198, v3, 4, v4
	v_bitop3_b32 v3, v6, v16, 4 bitop3:0x36
	s_lshl_b64 s[6:7], s[4:5], 22
	v_lshl_add_u32 v199, v3, 4, v12
	v_bitop3_b32 v3, v6, v11, 8 bitop3:0x36
	v_writelane_b32 v254, s9, 51
	s_add_u32 s9, s9, s6
	v_lshl_or_b32 v200, v3, 4, v4
	v_bitop3_b32 v3, v6, v16, 8 bitop3:0x36
	v_writelane_b32 v254, s10, 52
	s_addc_u32 s10, s10, s7
	s_lshl_b64 s[6:7], s[4:5], 14
	s_lshl_b32 s4, s70, 5
	v_lshl_add_u32 v201, v3, 4, v12
	v_bitop3_b32 v3, v6, v11, 12 bitop3:0x36
	s_add_i32 s5, s75, s4
	v_lshl_or_b32 v202, v3, 4, v4
	v_bitop3_b32 v3, v6, v16, 12 bitop3:0x36
	v_lshl_or_b32 v11, s70, 2, v2
	v_lshlrev_b32_e32 v2, 2, v0
	v_or_b32_e32 v178, s5, v1
	v_mov_b32_e32 v179, 0
	v_lshl_add_u32 v203, v3, 4, v12
	v_and_b32_e32 v12, 12, v2
	s_lshr_b32 s11, s85, 2
	v_lshl_add_u64 v[2:3], v[178:179], 2, s[6:7]
	v_and_or_b32 v2, s11, 3, v2
	v_lshlrev_b64 v[4:5], 8, v[2:3]
	v_lshl_add_u64 v[6:7], s[2:3], 0, v[4:5]
	v_lshlrev_b32_e32 v178, 4, v222
	v_lshl_add_u64 v[6:7], v[6:7], 0, v[178:179]
	s_waitcnt vmcnt(8)
	global_load_dwordx4 v[82:85], v[6:7], off offset:0 nt
	s_waitcnt vmcnt(7)
; #define ATT_DECODE(k_, b_, hd_, res_, ib_) do { const int u_ = F.vcu + (k_) * F.G; const int bh_ = u_ >> 4, uu_ = u_ & 15; b_ = bh_ >> 3; hd_ = bh_ & 7; res_ = uu_ / BPR; ib_ = (uu_ % BPR) * 1024; } while (0)
; template <int DIL, bool FIRST, bool LAST>
; DI void attn_phase(Frame& F) {
;     ...
;         { int b_, hd_, res_; ATT_DECODE(0, b_, hd_, res_, ib_i); kv_i = HMq + HM_PLANE + ((size_t)(b_ * 8 + hd_) * SEQ + res_) * 128; }
;     ...
;         u32x4 qfr[8], on[8]; u32x2 mlx; mlx.x = 0u; mlx.y = 0u;
;     ...
;         ATT_PREFETCH(0, F.wave);
; #pragma unroll
;         for (int jt = 0; jt < PRE; ++jt) ATT_ISSUE1();
	global_load_dwordx4 v[86:89], v[6:7], off offset:32 nt
	global_load_dwordx4 v[90:93], v[6:7], off offset:64 nt
	global_load_dwordx4 v[94:97], v[6:7], off offset:0x60 nt
	global_load_dwordx4 v[98:101], v[6:7], off offset:0x80 nt
	global_load_dwordx4 v[102:105], v[6:7], off offset:0xa0 nt
	global_load_dwordx4 v[106:109], v[6:7], off offset:0xc0 nt
	global_load_dwordx4 v[110:113], v[6:7], off offset:0xe0 nt
	v_lshl_add_u64 v[4:5], s[0:1], 0, v[4:5]
	v_lshl_add_u64 v[4:5], v[4:5], 0, v[178:179]
	global_load_dwordx4 v[114:117], v[4:5], off offset:0
	global_load_dwordx4 v[118:121], v[4:5], off offset:32
	global_load_dwordx4 v[122:125], v[4:5], off offset:64
	global_load_dwordx4 v[126:129], v[4:5], off offset:0x60
	global_load_dwordx4 v[130:133], v[4:5], off offset:0x80
	global_load_dwordx4 v[134:137], v[4:5], off offset:0xa0
	global_load_dwordx4 v[138:141], v[4:5], off offset:0xc0
	global_load_dwordx4 v[142:145], v[4:5], off offset:0xe0
	s_lshl_b32 s5, s85, 6
	v_lshl_add_u64 v[2:3], v[2:3], 3, s[76:77]
	v_add_u32_e32 v204, 0xffffff80, v11
	s_and_b32 s5, s5, 0x300
	global_load_dwordx2 v[180:181], v[2:3], off
	v_add_u32_e32 v3, s75, v204
	s_add_u32 s78, s9, s5
	v_max_i32_e32 v4, 0, v3
	v_mov_b32_e32 v5, v179
	s_addc_u32 s79, s10, 0
	v_lshlrev_b64 v[4:5], 10, v[4:5]
	v_lshl_add_u64 v[4:5], s[78:79], 0, v[4:5]
	v_lshlrev_b32_e32 v6, 4, v9
	v_mov_b32_e32 v7, v179
	v_lshl_add_u64 v[4:5], v[4:5], 0, v[6:7]
	s_mov_b64 s[80:81], 0x4000000
	s_add_i32 s96, s8, 0
	s_mov_b32 m0, s96
	global_load_lds_dwordx4 v[4:5], off nt
	v_lshl_add_u64 v[4:5], v[4:5], 0, s[80:81]
	s_add_i32 s5, s96, 0x2000
	s_mov_b32 m0, s5
	global_load_lds_dwordx4 v[4:5], off nt
	v_max_i32_e32 v4, 0xffffffe0, v3
	v_add_u32_e32 v4, 32, v4
	v_mov_b32_e32 v5, v179
	v_lshlrev_b64 v[4:5], 10, v[4:5]
	v_lshl_add_u64 v[4:5], s[78:79], 0, v[4:5]
	v_lshl_add_u64 v[4:5], v[4:5], 0, v[6:7]
	s_add_i32 s5, s96, 0x4000
	s_mov_b32 m0, s5
	global_load_lds_dwordx4 v[4:5], off nt
	v_lshl_add_u64 v[4:5], v[4:5], 0, s[80:81]
	s_addk_i32 s5, 0x2000
	s_mov_b32 m0, s5
	global_load_lds_dwordx4 v[4:5], off nt
	v_max_i32_e32 v4, 0xffffffc0, v3
	v_add_u32_e32 v4, 64, v4
	v_mov_b32_e32 v5, v179
	v_lshlrev_b64 v[4:5], 10, v[4:5]
	v_lshl_add_u64 v[4:5], s[78:79], 0, v[4:5]
	v_lshl_add_u64 v[4:5], v[4:5], 0, v[6:7]
	s_add_i32 s5, s96, 0x8000
	s_mov_b32 m0, s5
	global_load_lds_dwordx4 v[4:5], off nt
	v_lshl_add_u64 v[4:5], v[4:5], 0, s[80:81]
	s_addk_i32 s5, 0x2000
	s_mov_b32 m0, s5
	global_load_lds_dwordx4 v[4:5], off nt
	v_max_i32_e32 v4, 0xffffffa0, v3
	v_add_u32_e32 v4, 0x60, v4
	v_mov_b32_e32 v5, v179
	v_lshlrev_b64 v[4:5], 10, v[4:5]
	v_lshl_add_u64 v[4:5], s[78:79], 0, v[4:5]
	v_lshl_add_u64 v[4:5], v[4:5], 0, v[6:7]
	s_add_i32 s5, s96, 0xc000
	s_mov_b32 m0, s5
	global_load_lds_dwordx4 v[4:5], off nt
	v_lshl_add_u64 v[4:5], v[4:5], 0, s[80:81]
	s_addk_i32 s5, 0x2000
	s_mov_b32 m0, s5
	global_load_lds_dwordx4 v[4:5], off nt
	v_add_u32_e32 v4, s75, v11
	v_mov_b32_e32 v5, v179
	v_lshlrev_b64 v[4:5], 10, v[4:5]
	v_lshl_add_u64 v[4:5], s[78:79], 0, v[4:5]
	v_lshl_add_u64 v[4:5], v[4:5], 0, v[6:7]
	s_add_i32 s5, s96, 0x10000
	s_mov_b32 m0, s5
	global_load_lds_dwordx4 v[4:5], off nt
	v_lshl_add_u64 v[4:5], v[4:5], 0, s[80:81]
	v_max_i32_e32 v3, 0xffffff60, v3
	v_or_b32_e32 v14, v12, v8
	s_addk_i32 s5, 0x2000
	s_mov_b32 m0, s5
	global_load_lds_dwordx4 v[4:5], off nt
	v_add_u32_e32 v4, 0xa0, v3
	v_bitop3_b32 v3, v12, v222, v8 bitop3:0x36
	v_lshlrev_b32_e32 v206, 4, v3
	v_bitop3_b32 v3, v222, v14, 2 bitop3:0x36
	v_lshlrev_b32_e32 v207, 4, v3
	v_bitop3_b32 v3, v222, v14, 4 bitop3:0x36
	v_lshlrev_b32_e32 v208, 4, v3
	v_bitop3_b32 v3, v222, v14, 6 bitop3:0x36
	v_lshlrev_b32_e32 v209, 4, v3
	v_bitop3_b32 v3, v222, v14, 8 bitop3:0x36
	v_lshlrev_b32_e32 v210, 4, v3
	v_bitop3_b32 v3, v222, v14, 10 bitop3:0x36
	v_lshlrev_b32_e32 v211, 4, v3
	v_bitop3_b32 v3, v222, v14, 12 bitop3:0x36
	v_lshlrev_b32_e32 v212, 4, v3
	v_bitop3_b32 v3, v222, v14, 14 bitop3:0x36
	v_lshlrev_b32_e32 v213, 4, v3
	v_or_b32_e32 v3, 1, v10
	v_cmp_lt_u32_e64 s[8:9], v3, v1
	v_or_b32_e32 v3, 2, v10
	v_cmp_lt_u32_e64 s[12:13], v3, v1
	v_cmp_gt_u32_e64 s[14:15], v3, v1
	v_or_b32_e32 v3, 3, v10
	v_cmp_lt_u32_e64 s[16:17], v3, v1
	v_cmp_gt_u32_e64 s[18:19], v3, v1
	v_or_b32_e32 v3, 9, v10
	v_cmp_lt_u32_e64 s[24:25], v3, v1
	v_cmp_gt_u32_e64 s[26:27], v3, v1
	v_or_b32_e32 v3, 10, v10
	v_cmp_lt_u32_e64 s[28:29], v3, v1
	v_cmp_gt_u32_e64 s[30:31], v3, v1
	v_or_b32_e32 v3, 11, v10
	v_cmp_lt_u32_e64 s[34:35], v3, v1
	v_cmp_gt_u32_e64 s[36:37], v3, v1
	v_or_b32_e32 v3, 16, v10
	v_cmp_lt_u32_e64 s[38:39], v3, v1
	v_cmp_gt_u32_e64 s[40:41], v3, v1
	v_or_b32_e32 v3, 17, v10
	v_mov_b32_e32 v5, v179
	v_lshl_add_u64 v[182:183], s[0:1], 0, v[178:179]
	v_cmp_gt_u32_e64 s[0:1], 32, v224
	v_cmp_lt_u32_e64 s[42:43], v3, v1
	v_cmp_gt_u32_e64 s[44:45], v3, v1
	v_or_b32_e32 v3, 18, v10
	v_lshlrev_b64 v[4:5], 10, v[4:5]
	v_writelane_b32 v254, s0, 54
	v_cmp_lt_u32_e64 s[46:47], v3, v1
	v_cmp_gt_u32_e64 s[48:49], v3, v1
	v_or_b32_e32 v3, 19, v10
	v_lshl_add_u64 v[4:5], s[78:79], 0, v[4:5]
	v_writelane_b32 v254, s1, 55
	v_cmp_lt_u32_e64 s[0:1], v10, v1
	v_cmp_lt_u32_e64 s[50:51], v3, v1
	v_cmp_gt_u32_e64 s[52:53], v3, v1
	v_or_b32_e32 v3, 24, v10
	v_lshl_add_u64 v[4:5], v[4:5], 0, v[6:7]
	s_add_i32 s5, s96, 0x14000
	s_mov_b32 m0, s5
	global_load_lds_dwordx4 v[4:5], off nt
	v_writelane_b32 v254, s0, 56
	v_cmp_lt_u32_e64 s[54:55], v3, v1
	v_cmp_gt_u32_e64 s[56:57], v3, v1
	v_or_b32_e32 v3, 25, v10
	v_lshlrev_b32_e32 v2, 3, v9
	v_lshl_add_u64 v[4:5], v[4:5], 0, s[80:81]
	s_addk_i32 s5, 0x2000
	s_mov_b32 m0, s5
	global_load_lds_dwordx4 v[4:5], off nt
	v_writelane_b32 v254, s1, 57
	v_cmp_gt_u32_e64 s[0:1], v10, v1
	v_cmp_lt_u32_e64 s[58:59], v3, v1
	v_cmp_gt_u32_e64 s[60:61], v3, v1
	v_or_b32_e32 v3, 26, v10
	v_writelane_b32 v254, s0, 61
	v_cmp_lt_u32_e64 s[62:63], v3, v1
	v_cmp_gt_u32_e64 s[64:65], v3, v1
	v_or_b32_e32 v3, 27, v10
	v_lshlrev_b32_e32 v186, 1, v2
	v_mbcnt_lo_u32_b32 v2, -1, 0
	s_mov_b32 s97, 0
	s_mov_b32 s33, 6
	v_lshl_add_u64 v[184:185], s[2:3], 0, v[178:179]
	v_lshlrev_b32_e32 v205, 8, v1
	v_sub_u32_e32 v214, 0, v10
	v_writelane_b32 v254, s1, 62
	v_cmp_ge_u32_e64 s[10:11], v10, v1
	v_sub_u32_e32 v215, -8, v10
	v_cmp_lt_u32_e64 s[20:21], v13, v1
	v_cmp_gt_u32_e64 s[22:23], v13, v1
	v_xor_b32_e32 v216, -9, v10
	v_xor_b32_e32 v217, -10, v10
	v_xor_b32_e32 v218, -11, v10
	v_sub_u32_e32 v219, -16, v10
	v_xor_b32_e32 v220, 0xffffffef, v10
	v_xor_b32_e32 v221, 0xffffffee, v10
	v_xor_b32_e32 v222, 0xffffffed, v10
	v_sub_u32_e32 v223, 0xffffffe8, v10
	v_xor_b32_e32 v225, 0xffffffe7, v10
	v_xor_b32_e32 v226, 0xffffffe6, v10
	v_xor_b32_e32 v227, 0xffffffe5, v10
	v_cmp_lt_u32_e64 s[66:67], v3, v1
	v_cmp_gt_u32_e64 s[68:69], v3, v1
	v_or_b32_e32 v228, s4, v1
	v_or_b32_e32 v229, 0x100, v1
	s_sub_i32 s84, 0, s70
	v_mov_b32_e32 v230, 0xf149f2ca
	v_mbcnt_hi_u32_b32 v231, -1, v2
	s_mov_b32 s5, 6
	s_mov_b32 s6, 0
	v_mov_b32_e32 v194, 0xf149f2ca
	v_mov_b32_e32 v195, v179
	s_mov_b32 s7, 0
	s_waitcnt vmcnt(0)
	s_branch .LBB0_588

.LBB0_590:
	s_lshl_b32 s0, s33, 5
	s_add_i32 s0, s75, s0
	v_add_u32_e32 v66, s0, v204
	v_max_i32_e32 v178, 0, v66
	v_lshlrev_b64 v[66:67], 10, v[178:179]
	v_lshl_add_u64 v[66:67], s[78:79], 0, v[66:67]
	v_mov_b32_e32 v187, v179
	s_and_b32 s0, s73, 0x1c000
	v_lshl_add_u64 v[66:67], v[66:67], 0, v[186:187]
	s_add_i32 s0, s96, s0
	s_mov_b32 m0, s0
	global_load_lds_dwordx4 v[66:67], off nt
	v_lshl_add_u64 v[66:67], v[66:67], 0, s[80:81]
	s_addk_i32 s0, 0x2000
	s_mov_b32 m0, s0
	global_load_lds_dwordx4 v[66:67], off nt
	s_add_i32 s33, s33, 1
	s_cmp_lg_u32 s33, 36
	s_cbranch_scc1 .LBB0_593
	s_add_i32 s0, s97, 1
	s_cmp_ge_i32 s0, s72
	s_mov_b32 s33, 35
	s_cbranch_scc1 .LBB0_593
	v_readlane_b32 s1, v254, 2
	s_mul_i32 s1, s0, s1
	v_readlane_b32 s3, v254, 43
	s_add_i32 s1, s1, s3
	s_lshl_b32 s4, s1, 10
	s_and_b32 s75, s4, 0xc00
	s_ashr_i32 s4, s1, 4
	s_bfe_u32 s3, s1, 0x30004
	s_and_b32 s4, s4, -8
	s_or_b32 s4, s4, s3
	s_ashr_i32 s5, s4, 31
	s_lshl_b64 s[4:5], s[4:5], 22
	v_readlane_b32 s3, v254, 51
	s_add_u32 s3, s3, s4
	v_readlane_b32 s4, v254, 52
	s_addc_u32 s4, s4, s5
	s_lshl_b32 s1, s1, 6
	s_and_b32 s1, s1, 0x300
	s_add_u32 s78, s3, s1
	s_addc_u32 s79, s4, 0
	s_mov_b32 s33, 0
	s_mov_b32 s97, s0

; template <int DIL, bool FIRST, bool LAST>
; DI void attn_phase(Frame& F) {
;     ...
;                         if (mq < 3) ATT_PREFETCH(k, qt + 8); else if (k + 1 < nun) ATT_PREFETCH(k + 1, F.wave);
.LBB0_612:
	v_readlane_b32 s0, v254, 49
	v_readlane_b32 s1, v254, 50
	s_andn2_b64 vcc, exec, s[0:1]
	s_cbranch_vccnz .LBB0_614
	global_load_dwordx4 v[82:85], v[188:189], off offset:0 nt
	global_load_dwordx4 v[86:89], v[188:189], off offset:32 nt
	global_load_dwordx4 v[90:93], v[188:189], off offset:64 nt
	global_load_dwordx4 v[94:97], v[188:189], off offset:0x60 nt
	global_load_dwordx4 v[98:101], v[188:189], off offset:0x80 nt
	global_load_dwordx4 v[102:105], v[188:189], off offset:0xa0 nt
	global_load_dwordx4 v[106:109], v[188:189], off offset:0xc0 nt
	global_load_dwordx4 v[110:113], v[188:189], off offset:0xe0 nt
	global_load_dwordx4 v[114:117], v[190:191], off offset:0
	global_load_dwordx4 v[118:121], v[190:191], off offset:32
	global_load_dwordx4 v[122:125], v[190:191], off offset:64
	global_load_dwordx4 v[126:129], v[190:191], off offset:0x60
	global_load_dwordx4 v[130:133], v[190:191], off offset:0x80
	global_load_dwordx4 v[134:137], v[190:191], off offset:0xa0
	global_load_dwordx4 v[138:141], v[190:191], off offset:0xc0
	global_load_dwordx4 v[142:145], v[190:191], off offset:0xe0
	global_load_dwordx2 v[180:181], v[192:193], off

; template <int DIL, bool FIRST, bool LAST>
; DI void attn_phase(Frame& F) {
;     ...
;                         if (mq < 3) ATT_PREFETCH(k, qt + 8); else if (k + 1 < nun) ATT_PREFETCH(k + 1, F.wave);
.LBB0_615:
	v_add_u32_e32 v66, s4, v232
	v_ashrrev_i32_e32 v67, 31, v66
	v_lshl_add_u64 v[66:67], v[66:67], 2, s[82:83]
	v_lshlrev_b64 v[68:69], 8, v[66:67]
	v_lshl_add_u64 v[70:71], v[184:185], 0, v[68:69]
	global_load_dwordx4 v[82:85], v[70:71], off offset:0 nt
	global_load_dwordx4 v[86:89], v[70:71], off offset:32 nt
	global_load_dwordx4 v[90:93], v[70:71], off offset:64 nt
	global_load_dwordx4 v[94:97], v[70:71], off offset:0x60 nt
	global_load_dwordx4 v[98:101], v[70:71], off offset:0x80 nt
	global_load_dwordx4 v[102:105], v[70:71], off offset:0xa0 nt
	global_load_dwordx4 v[106:109], v[70:71], off offset:0xc0 nt
	global_load_dwordx4 v[110:113], v[70:71], off offset:0xe0 nt
	v_lshl_add_u64 v[68:69], v[182:183], 0, v[68:69]
	global_load_dwordx4 v[114:117], v[68:69], off offset:0
	global_load_dwordx4 v[118:121], v[68:69], off offset:32
	global_load_dwordx4 v[122:125], v[68:69], off offset:64
	global_load_dwordx4 v[126:129], v[68:69], off offset:0x60
	global_load_dwordx4 v[130:133], v[68:69], off offset:0x80
	global_load_dwordx4 v[134:137], v[68:69], off offset:0xa0
	global_load_dwordx4 v[138:141], v[68:69], off offset:0xc0
	global_load_dwordx4 v[142:145], v[68:69], off offset:0xe0
	v_lshl_add_u64 v[66:67], v[66:67], 3, s[76:77]
	global_load_dwordx2 v[180:181], v[66:67], off
	s_branch .LBB0_589
